# first-arriving workgroup of each XCD starts an extra early L2 write-back at the grid barrier (on top of the flattened release)
# baseline (speedup 1.0000x reference)
; __device__ __forceinline__ unsigned xb_ld(unsigned* p)              { return __hip_atomic_load(p, __ATOMIC_RELAXED, __HIP_MEMORY_SCOPE_AGENT); }
; __device__ __forceinline__ unsigned xb_add(unsigned* p, unsigned v) { return __hip_atomic_fetch_add(p, v, __ATOMIC_RELAXED, __HIP_MEMORY_SCOPE_AGENT); }
; #define XB_SPIN(cond, bar) do { unsigned _sp = 0; while (cond) { __builtin_amdgcn_s_sleep(1); \
;     if ((++_sp & 255u) == 0u) { if (xb_ld(&(bar)[XB_TMO])) break; if (_sp > XB_SPIN_CAP) { atomicAdd(&(bar)[XB_TMO], 1u); break; } } } } while (0)
; __device__ __forceinline__ void xcd_barrier(const XcdBarrier& b) {
;     ...
;         const unsigned old = xb_add(&bar[XB_XSUB(b.x)], 1u);
;         const unsigned gen = old / nloc;
;         if (old + 1u == (gen + 1u) * nloc) {
;             __builtin_amdgcn_fence(__ATOMIC_RELEASE, "agent");
;             asm volatile("s_waitcnt vmcnt(0)" ::: "memory");
;             const unsigned og = xb_add(&bar[XB_TOP], 1u);
;             const unsigned tg = og / nx;
;             if (og + 1u == (tg + 1u) * nx) xb_add(&bar[XB_TOPGEN], 1u);
;             else XB_SPIN(xb_ld(&bar[XB_TOPGEN]) == tg, bar);
;             __builtin_amdgcn_fence(__ATOMIC_ACQUIRE, "agent");
;             xb_add(&bar[XB_XGEN(b.x)], 1u);
;             asm volatile("s_waitcnt vmcnt(0)" ::: "memory");
;         } else {
;             XB_SPIN(xb_ld(&bar[XB_XGEN(b.x)]) == gen, bar);
.LBB0_455:
	v_readlane_b32 s4, v254, 17
	v_readlane_b32 s5, v254, 18
	v_cvt_f32_u32_e32 v1, v4
	v_sub_u32_e32 v6, 0, v4
	v_rcp_iflag_f32_e32 v1, v1
	s_nop 1
	global_atomic_add v5, v3, v244, s[4:5] sc0
	v_mul_f32_e32 v1, 0x4f7ffffe, v1
	v_cvt_u32_f32_e32 v1, v1
	v_mul_lo_u32 v6, v6, v1
	v_mul_hi_u32 v6, v1, v6
	v_add_u32_e32 v1, v1, v6
	s_waitcnt vmcnt(0)
	v_mul_hi_u32 v1, v5, v1
	v_mul_lo_u32 v6, v1, v4
	v_sub_u32_e32 v6, v5, v6
	v_add_u32_e32 v7, 1, v1
	v_cmp_ge_u32_e32 vcc, v6, v4
	v_add_u32_e32 v5, 1, v5
	s_nop 0
	v_cndmask_b32_e32 v1, v1, v7, vcc
	v_sub_u32_e32 v7, v6, v4
	v_cndmask_b32_e32 v6, v6, v7, vcc
	v_add_u32_e32 v7, 1, v1
	v_cmp_ge_u32_e32 vcc, v6, v4
	s_nop 1
	v_cndmask_b32_e32 v1, v1, v7, vcc
	v_mul_lo_u32 v6, v4, v1
	v_add_u32_e32 v7, 1, v6
	v_cmp_eq_u32_e32 vcc, v5, v7
	s_cbranch_vccz .Learlywb_0
	buffer_wbl2 sc1
.Learlywb_0:
	v_add_u32_e32 v4, v6, v4
	v_cmp_ne_u32_e32 vcc, v5, v4
	s_and_saveexec_b64 s[4:5], vcc
	s_xor_b64 s[44:45], exec, s[4:5]
	s_cbranch_execz .LBB0_469
	v_readlane_b32 s4, v254, 23
	v_readlane_b32 s5, v254, 24
	s_waitcnt lgkmcnt(0)
	s_nop 3
	global_load_dword v2, v3, s[4:5] sc1
	s_waitcnt vmcnt(0)
	v_cmp_eq_u32_e32 vcc, v2, v1
	s_and_saveexec_b64 s[48:49], vcc
	s_cbranch_execz .LBB0_468
	s_mov_b32 s18, 1
	s_mov_b64 s[4:5], 0
	s_branch .LBB0_459

; __device__ __forceinline__ unsigned xb_ld(unsigned* p)              { return __hip_atomic_load(p, __ATOMIC_RELAXED, __HIP_MEMORY_SCOPE_AGENT); }
; __device__ __forceinline__ unsigned xb_add(unsigned* p, unsigned v) { return __hip_atomic_fetch_add(p, v, __ATOMIC_RELAXED, __HIP_MEMORY_SCOPE_AGENT); }
; #define XB_SPIN(cond, bar) do { unsigned _sp = 0; while (cond) { __builtin_amdgcn_s_sleep(1); \
;     if ((++_sp & 255u) == 0u) { if (xb_ld(&(bar)[XB_TMO])) break; if (_sp > XB_SPIN_CAP) { atomicAdd(&(bar)[XB_TMO], 1u); break; } } } } while (0)
; __device__ __forceinline__ void xcd_barrier(const XcdBarrier& b) {
;     ...
;         const unsigned old = xb_add(&bar[XB_XSUB(b.x)], 1u);
;         const unsigned gen = old / nloc;
;         if (old + 1u == (gen + 1u) * nloc) {
;             __builtin_amdgcn_fence(__ATOMIC_RELEASE, "agent");
;             asm volatile("s_waitcnt vmcnt(0)" ::: "memory");
;             const unsigned og = xb_add(&bar[XB_TOP], 1u);
;             const unsigned tg = og / nx;
;             if (og + 1u == (tg + 1u) * nx) xb_add(&bar[XB_TOPGEN], 1u);
;             else XB_SPIN(xb_ld(&bar[XB_TOPGEN]) == tg, bar);
;             __builtin_amdgcn_fence(__ATOMIC_ACQUIRE, "agent");
;             xb_add(&bar[XB_XGEN(b.x)], 1u);
;             asm volatile("s_waitcnt vmcnt(0)" ::: "memory");
;         } else {
;             XB_SPIN(xb_ld(&bar[XB_XGEN(b.x)]) == gen, bar);
.Learlywb_1:
	v_add_u32_e32 v4, v6, v4
	v_cmp_ne_u32_e32 vcc, v5, v4
	s_and_saveexec_b64 s[4:5], vcc
	s_xor_b64 s[40:41], exec, s[4:5]
	s_cbranch_execz .LBB0_562
	v_readlane_b32 s4, v254, 23
	v_readlane_b32 s5, v254, 24
	s_waitcnt lgkmcnt(0)
	s_nop 3
	global_load_dword v2, v3, s[4:5] sc1
	s_waitcnt vmcnt(0)
	v_cmp_eq_u32_e32 vcc, v2, v1
	s_and_saveexec_b64 s[42:43], vcc
	s_cbranch_execz .LBB0_561
	s_mov_b32 s18, 1
	s_mov_b64 s[4:5], 0
	s_branch .LBB0_552

; __device__ __forceinline__ unsigned xb_ld(unsigned* p)              { return __hip_atomic_load(p, __ATOMIC_RELAXED, __HIP_MEMORY_SCOPE_AGENT); }
; __device__ __forceinline__ unsigned xb_add(unsigned* p, unsigned v) { return __hip_atomic_fetch_add(p, v, __ATOMIC_RELAXED, __HIP_MEMORY_SCOPE_AGENT); }
; #define XB_SPIN(cond, bar) do { unsigned _sp = 0; while (cond) { __builtin_amdgcn_s_sleep(1); \
;     if ((++_sp & 255u) == 0u) { if (xb_ld(&(bar)[XB_TMO])) break; if (_sp > XB_SPIN_CAP) { atomicAdd(&(bar)[XB_TMO], 1u); break; } } } } while (0)
; __device__ __forceinline__ void xcd_barrier(const XcdBarrier& b) {
;     ...
;         const unsigned old = xb_add(&bar[XB_XSUB(b.x)], 1u);
;         const unsigned gen = old / nloc;
;         if (old + 1u == (gen + 1u) * nloc) {
;             __builtin_amdgcn_fence(__ATOMIC_RELEASE, "agent");
;             asm volatile("s_waitcnt vmcnt(0)" ::: "memory");
;             const unsigned og = xb_add(&bar[XB_TOP], 1u);
;             const unsigned tg = og / nx;
;             if (og + 1u == (tg + 1u) * nx) xb_add(&bar[XB_TOPGEN], 1u);
;             else XB_SPIN(xb_ld(&bar[XB_TOPGEN]) == tg, bar);
;             __builtin_amdgcn_fence(__ATOMIC_ACQUIRE, "agent");
;             xb_add(&bar[XB_XGEN(b.x)], 1u);
;             asm volatile("s_waitcnt vmcnt(0)" ::: "memory");
;         } else {
;             XB_SPIN(xb_ld(&bar[XB_XGEN(b.x)]) == gen, bar);
.Learlywb_6:
	v_add_u32_e32 v4, v6, v4
	v_cmp_ne_u32_e32 vcc, v5, v4
	s_and_saveexec_b64 s[4:5], vcc
	s_xor_b64 s[40:41], exec, s[4:5]
	s_cbranch_execz .LBB0_1552
	v_readlane_b32 s4, v254, 23
	v_readlane_b32 s5, v254, 24
	s_waitcnt lgkmcnt(0)
	s_nop 3
	global_load_dword v2, v3, s[4:5] sc1
	s_waitcnt vmcnt(0)
	v_cmp_eq_u32_e32 vcc, v2, v1
	s_and_saveexec_b64 s[42:43], vcc
	s_cbranch_execz .LBB0_1551
	s_mov_b32 s17, 1
	s_mov_b64 s[4:5], 0
	s_branch .LBB0_1542

; __device__ __forceinline__ unsigned xb_ld(unsigned* p)              { return __hip_atomic_load(p, __ATOMIC_RELAXED, __HIP_MEMORY_SCOPE_AGENT); }
; __device__ __forceinline__ unsigned xb_add(unsigned* p, unsigned v) { return __hip_atomic_fetch_add(p, v, __ATOMIC_RELAXED, __HIP_MEMORY_SCOPE_AGENT); }
; #define XB_SPIN(cond, bar) do { unsigned _sp = 0; while (cond) { __builtin_amdgcn_s_sleep(1); \
;     if ((++_sp & 255u) == 0u) { if (xb_ld(&(bar)[XB_TMO])) break; if (_sp > XB_SPIN_CAP) { atomicAdd(&(bar)[XB_TMO], 1u); break; } } } } while (0)
; __device__ __forceinline__ void xcd_barrier(const XcdBarrier& b) {
;     ...
;         const unsigned old = xb_add(&bar[XB_XSUB(b.x)], 1u);
;         const unsigned gen = old / nloc;
;         if (old + 1u == (gen + 1u) * nloc) {
;             __builtin_amdgcn_fence(__ATOMIC_RELEASE, "agent");
;             asm volatile("s_waitcnt vmcnt(0)" ::: "memory");
;             const unsigned og = xb_add(&bar[XB_TOP], 1u);
;             const unsigned tg = og / nx;
;             if (og + 1u == (tg + 1u) * nx) xb_add(&bar[XB_TOPGEN], 1u);
;             else XB_SPIN(xb_ld(&bar[XB_TOPGEN]) == tg, bar);
;             __builtin_amdgcn_fence(__ATOMIC_ACQUIRE, "agent");
;             xb_add(&bar[XB_XGEN(b.x)], 1u);
;             asm volatile("s_waitcnt vmcnt(0)" ::: "memory");
;         } else {
;             XB_SPIN(xb_ld(&bar[XB_XGEN(b.x)]) == gen, bar);
.Learlywb_9:
	v_add_u32_e32 v4, v6, v4
	v_cmp_ne_u32_e32 vcc, v5, v4
	s_and_saveexec_b64 s[4:5], vcc
	s_xor_b64 s[44:45], exec, s[4:5]
	s_cbranch_execz .LBB0_1792
	v_readlane_b32 s4, v254, 23
	v_readlane_b32 s5, v254, 24
	s_waitcnt lgkmcnt(0)
	s_nop 3
	global_load_dword v2, v3, s[4:5] sc1
	s_waitcnt vmcnt(0)
	v_cmp_eq_u32_e32 vcc, v2, v1
	s_and_saveexec_b64 s[46:47], vcc
	s_cbranch_execz .LBB0_1791
	s_mov_b32 s17, 1
	s_mov_b64 s[4:5], 0
	s_branch .LBB0_1765
